# v38 + M2 GLA state lines dealt to waves 0-3 of every workgroup instead of all waves of workgroups 0-127
# speedup vs baseline: 1.0028x; 1.0028x over previous
; __device__ __forceinline__ void m2_phase(KA A, int wave, int lane, int bid, int G) {
;     ...
;     float* CSG = (float*)(ws + WS_CSG); const float* GL = (const float*)(ws + WS_GLAST);
;     for (int line = gw; line < BATCH * 2 * 4 * 64; line += NGW) {
;         const int k = line & 63, h = (line >> 6) & 3, d = (line >> 8) & 1, b = line >> 9;
;         float s0 = 0.f, s1 = 0.f;
; #pragma unroll
;         for (int half = 0; half < 2; ++half) {
;             float c0[34], c1[34], dc[34];
; #pragma unroll
;             for (int ii = 0; ii < 34; ++ii) { const int i = half * 34 + ii; const int c = d == 0 ? i : (i < 4 ? 3 - i : NCH_G + 3 - i);
;                 const float* cs = CSG + (((((size_t)b * NCH_G + c) * 2 + d) * 4 + h) * 64 + k) * 128;
;                 c0[ii] = cs[lane]; c1[ii] = cs[lane + 64]; dc[ii] = GL[((((size_t)b * NCH_G + c) * 2 + d) * 4 + h) * 64 + k]; }
.LBB0_1340:
	s_and_b32 s100, s12, 4
	s_cmp_lg_u32 s100, 0
	s_cbranch_scc1 .LBB0_1343
	s_lshr_b32 s100, s12, 3
	s_and_b32 s12, s12, 3
	s_lshl2_add_u32 s12, s100, s12
	s_cmpk_gt_i32 s12, 0x3ff
	s_cbranch_scc1 .LBB0_1343
	s_waitcnt lgkmcnt(0)
	s_add_u32 s16, s0, 0xc10000
	v_mov_b32_e32 v3, v130
	v_mov_b32_e32 v5, v130
	s_addc_u32 s17, s1, 0
	v_lshl_add_u64 v[2:3], s[0:1], 0, v[2:3]
	s_mov_b64 s[4:5], 0x45e00000
	v_lshl_add_u64 v[4:5], s[0:1], 0, v[4:5]
	s_mov_b64 s[0:1], 0x49c00000
	v_lshl_add_u64 v[2:3], v[2:3], 0, s[4:5]
	v_lshl_add_u64 v[4:5], v[4:5], 0, s[0:1]
	v_writelane_b32 v255, vcc_lo, 0
